# static s_setprio 1 for waves 0-3 across the attention/conversion ticket loop (reset after the loop)
# speedup vs baseline: 1.0114x; 1.0011x over previous
; __device__ __forceinline__ Ptrs make_ptrs(const Args& args, unsigned char* ws0) {
;     int z = 0; asm volatile("" : "+s"(z));
;     const float* const* in = args.in + z;
;     unsigned char* ws = ws0 + z;
;     Ptrs P;
;     P.x = in[0]; P.attn_norm = in[1]; P.w_in = in[2]; P.q_gain = in[3]; P.k_gain = in[4]; P.out_gain = in[5]; P.w_out = in[6]; P.ffn_norm = in[7];
;     P.dwg = in[8]; P.dwu = in[9]; P.dwd = in[10]; P.router = in[11]; P.mwg = in[12]; P.mwu = in[13]; P.mwd = in[14];
;     P.out = args.out; P.ctl = (gu32*)(ws + WS_CTL);
;     P.Wqkv_t = (bf16*)(ws + WS_WQKV); P.Wo_t = (bf16*)(ws + WS_WO); P.Wgu_d = ws + WS_WGU_D; P.Wd_d = ws + WS_WD_D; P.Wgu_m = ws + WS_WGU_M; P.Wd_m = ws + WS_WD_M;
;     P.QKV = (bf16*)(ws + WS_QKV); P.OB = (bf16*)(ws + WS_O); P.AB = (bf16*)(ws + WS_A); P.AB8 = ws + WS_A; P.ACT = ws + WS_ACT; P.XS = ws + WS_XS;
;     P.H = (bf16*)(ws + WS_H); P.YS = (bf16*)(ws + WS_YS); P.kmean = (float*)(ws + WS_MISC + MISC_KMEAN); P.DPO = (bf16*)(ws + WS_DPO); P.DPL = (float*)(ws + WS_DPL);
;     P.rsq = (float*)(ws + WS_MISC + MISC_RSQ); P.Wv8 = ws + WS_WV8;
;     P.sel_e = (unsigned*)(ws + WS_MISC + MISC_SELE); P.sel_rel = (int*)(ws + WS_MISC + MISC_SELREL); P.sel_g = (float*)(ws + WS_MISC + MISC_SELG); P.sel_pos = (int*)(ws + WS_MISC + MISC_SELPOS);
;     return P;
; __global__ void __launch_bounds__(NWAVES * 64, 2) hybrid_fwd(Args args) {
;     ...
;             const Ptrs P = make_ptrs(args, ws0);
;             const att::AttnArgs AA{P.QKV, P.OB, P.kmean, P.out_gain + layer * D, P.DPO, P.DPL, (unsigned*)((unsigned char*)P.DPL + (WS_MLIST - WS_DPL)) + (size_t)layer * att::N_SEL * att::MLCAP, (unsigned*)(P.ctl + CW_MCNT + 256 * (layer + args.qoff)), (unsigned*)(P.ctl + CW_MDONE + 64 * (layer + args.qoff)), (layer == WO8_LAYER) ? 1 : 0};
;     ...
;             attn_conv_phase(P, AA, layer, (unsigned*)(P.ctl + CW_ATTQ + 64 * (layer + args.qoff)), lds, wave);
.LBB0_434:
	s_or_b64 exec, exec, s[14:15]
	s_add_u32 s3, s20, 0x8300000
	s_addc_u32 s81, s21, 0
	v_writelane_b32 v254, s3, 57
	s_add_u32 s3, s20, 0x1e300000
	v_writelane_b32 v254, s3, 58
	s_addc_u32 s3, s21, 0
	s_add_u32 s38, s20, 0x2d300000
	s_addc_u32 s39, s21, 0
	v_writelane_b32 v254, s3, 59
	s_add_u32 s3, s20, 0x33300000
	v_writelane_b32 v254, s3, 60
	s_addc_u32 s3, s21, 0
	v_writelane_b32 v254, s3, 61
	s_add_u32 s3, s20, 0x48100000
	v_writelane_b32 v254, s3, 62
	s_addc_u32 s3, s21, 0
	s_add_u32 s92, s20, 0x48200000
	s_addc_u32 s93, s21, 0
	s_add_u32 s14, s20, 0x4da00000
	s_addc_u32 s15, s21, 0
	v_writelane_b32 v255, s14, 0
	v_writelane_b32 v254, s3, 63
	s_nop 0
	v_writelane_b32 v255, s15, 1
	s_add_u32 s14, s20, 0x4e100000
	s_addc_u32 s15, s21, 0
	v_writelane_b32 v255, s14, 2
	s_nop 1
	v_writelane_b32 v255, s15, 3
	s_lshl_b32 s14, s80, 11
	s_mov_b32 s15, s90
	s_lshl_b64 s[14:15], s[14:15], 2
	s_add_u32 s14, s44, s14
	s_addc_u32 s15, s45, s15
	v_writelane_b32 v255, s14, 6
	s_nop 1
	v_writelane_b32 v255, s15, 7
	s_mul_i32 s14, s80, 0x8ca00
	s_mov_b32 s15, s90
	s_lshl_b64 s[14:15], s[14:15], 2
	s_add_u32 s14, s20, s14
	s_addc_u32 s15, s21, s15
	s_add_u32 s14, s14, 0x4dc00000
	s_addc_u32 s15, s15, 0
	v_writelane_b32 v255, s14, 8
	s_nop 1
	v_writelane_b32 v255, s15, 9
	s_lshl_b32 s14, s22, 8
	s_ashr_i32 s15, s14, 31
	s_lshl_b64 s[14:15], s[14:15], 2
	s_add_u32 s14, s20, s14
	s_addc_u32 s15, s21, s15
	s_add_u32 s14, s14, 0x9000
	s_addc_u32 s15, s15, 0
	s_add_u32 s0, s20, s0
	s_addc_u32 s1, s21, s1
	s_add_u32 s78, s0, 0xa000
	s_addc_u32 s79, s1, 0
	v_writelane_b32 v255, s14, 10
	s_add_u32 s0, s46, 0x1000000
	s_addc_u32 s1, s47, 0
	v_writelane_b32 v255, s15, 11
	v_writelane_b32 v255, s0, 12
	s_nop 1
	v_writelane_b32 v255, s1, 13
	s_add_u32 s0, s20, 0x3900000
	s_addc_u32 s1, s21, 0
	v_writelane_b32 v255, s0, 14
	s_mov_b64 s[20:21], 0
	s_nop 0
	v_writelane_b32 v255, s1, 15
	s_add_u32 s0, s40, 0x2000
	s_addc_u32 s1, s41, 0
	v_writelane_b32 v255, s0, 16
	s_nop 1
	v_writelane_b32 v255, s1, 17
	s_add_u32 s0, s42, 0x3000000
	s_addc_u32 s1, s43, 0
	v_writelane_b32 v255, s0, 18
	s_nop 1
	v_writelane_b32 v255, s1, 19
	v_writelane_b32 v255, s38, 20
	s_nop 1
	v_writelane_b32 v255, s39, 21
	v_writelane_b32 v255, s78, 22
	s_nop 1
	v_writelane_b32 v255, s79, 23
	s_cmpk_lt_u32 s94, 0x100
	s_cbranch_scc0 .Lprio_att_done
	s_setprio 1
